# MLA up-projection epilogue: t1 tile load issued together with the e4m3 gate load (fresh registers), one wait per half-step
# baseline (speedup 1.0000x reference)
.LBB0_1377:
	v_lshl_add_u32 v2, s2, 8, v1
	s_lshl_b32 s10, s4, 8
	v_ashrrev_i32_e32 v3, 31, v2
	s_ashr_i32 s11, s10, 31
	v_lshlrev_b64 v[4:5], 11, v[2:3]
	v_lshl_add_u64 v[4:5], v[4:5], 0, s[10:11]
	v_readlane_b32 s64, v237, 61
	v_or_b32_e32 v6, v4, v170
	v_mov_b32_e32 v7, v5
	v_readlane_b32 s70, v238, 3
	v_readlane_b32 s71, v238, 4
	s_nop 15
	s_nop 15
	s_nop 15
	v_pk_mul_f32 v[10:11], v[160:161], s[22:23] op_sel_hi:[1,0]
	v_pk_mul_f32 v[14:15], v[158:159], s[22:23] op_sel_hi:[1,0]
	v_lshl_add_u64 v[8:9], s[70:71], 0, v[6:7]
	global_load_dwordx2 v[8:9], v[8:9], off
	v_lshl_add_u64 v[196:197], v[6:7], 1, s[62:63]
	global_load_dwordx4 v[192:195], v[196:197], off
	v_pk_mul_f32 v[16:17], v[156:157], s[22:23] op_sel_hi:[1,0]
	v_pk_mul_f32 v[18:19], v[154:155], s[22:23] op_sel_hi:[1,0]
	v_cndmask_b32_e64 v3, 0, 1, s[18:19]
	v_cmp_ne_u32_e64 s[2:3], 1, v3
	s_andn2_b64 vcc, exec, s[18:19]
	v_readlane_b32 s65, v237, 62
	v_readlane_b32 s66, v237, 63
	v_readlane_b32 s67, v238, 0
	v_readlane_b32 s68, v238, 1
	v_readlane_b32 s69, v238, 2
	v_readlane_b32 s72, v238, 5
	v_readlane_b32 s73, v238, 6
	v_readlane_b32 s74, v238, 7
	v_readlane_b32 s75, v238, 8
	v_readlane_b32 s76, v238, 9
	v_readlane_b32 s77, v238, 10
	v_readlane_b32 s78, v238, 11
	v_readlane_b32 s79, v238, 12
	s_waitcnt vmcnt(0)
	v_cvt_pk_f32_fp8_sdwa v[12:13], v8 src0_sel:WORD_1
	v_cvt_pk_f32_fp8_e32 v[20:21], v8
	v_cvt_pk_f32_fp8_sdwa v[22:23], v9 src0_sel:WORD_1
	v_cvt_pk_f32_fp8_e32 v[24:25], v9
	v_pk_mul_f32 v[12:13], v[10:11], v[12:13]
	v_pk_mul_f32 v[14:15], v[14:15], v[20:21]
	v_pk_mul_f32 v[8:9], v[16:17], v[22:23]
	v_pk_mul_f32 v[10:11], v[18:19], v[24:25]
	s_cbranch_vccnz .LBB0_1379
	v_lshlrev_b32_e32 v20, 16, v192
	v_and_b32_e32 v21, 0xffff0000, v192
	v_lshlrev_b32_e32 v16, 16, v193
	v_and_b32_e32 v17, 0xffff0000, v193
	v_lshlrev_b32_e32 v22, 16, v194
	v_and_b32_e32 v23, 0xffff0000, v194
	v_lshlrev_b32_e32 v18, 16, v195
	v_and_b32_e32 v19, 0xffff0000, v195
	v_pk_add_f32 v[12:13], v[12:13], v[16:17]
	v_pk_add_f32 v[14:15], v[14:15], v[20:21]
	v_pk_add_f32 v[8:9], v[8:9], v[18:19]
	v_pk_add_f32 v[10:11], v[10:11], v[22:23]

.LBB0_1382:
	v_readlane_b32 s64, v237, 61
	v_lshl_add_u64 v[4:5], v[4:5], 0, v[170:171]
	v_readlane_b32 s70, v238, 3
	v_readlane_b32 s71, v238, 4
	v_pk_mul_f32 v[8:9], v[152:153], s[22:23] op_sel_hi:[1,0]
	v_pk_mul_f32 v[12:13], v[150:151], s[22:23] op_sel_hi:[1,0]
	v_lshl_add_u64 v[6:7], s[70:71], 0, v[4:5]
	global_load_dwordx2 v[6:7], v[6:7], off offset:128
	v_lshl_add_u64 v[196:197], v[4:5], 1, s[62:63]
	global_load_dwordx4 v[192:195], v[196:197], off offset:256
	v_pk_mul_f32 v[14:15], v[148:149], s[22:23] op_sel_hi:[1,0]
	v_pk_mul_f32 v[16:17], v[146:147], s[22:23] op_sel_hi:[1,0]
	s_and_b64 vcc, exec, s[2:3]
	v_readlane_b32 s65, v237, 62
	v_readlane_b32 s66, v237, 63
	v_readlane_b32 s67, v238, 0
	v_readlane_b32 s68, v238, 1
	v_readlane_b32 s69, v238, 2
	v_readlane_b32 s72, v238, 5
	v_readlane_b32 s73, v238, 6
	v_readlane_b32 s74, v238, 7
	v_readlane_b32 s75, v238, 8
	v_readlane_b32 s76, v238, 9
	v_readlane_b32 s77, v238, 10
	v_readlane_b32 s78, v238, 11
	v_readlane_b32 s79, v238, 12
	s_waitcnt vmcnt(0)
	v_cvt_pk_f32_fp8_sdwa v[10:11], v6 src0_sel:WORD_1
	v_cvt_pk_f32_fp8_e32 v[18:19], v6
	v_cvt_pk_f32_fp8_sdwa v[20:21], v7 src0_sel:WORD_1
	v_cvt_pk_f32_fp8_e32 v[22:23], v7
	v_pk_mul_f32 v[10:11], v[8:9], v[10:11]
	v_pk_mul_f32 v[12:13], v[12:13], v[18:19]
	v_pk_mul_f32 v[6:7], v[14:15], v[20:21]
	v_pk_mul_f32 v[8:9], v[16:17], v[22:23]
	s_cbranch_vccnz .LBB0_1384
	v_lshlrev_b32_e32 v18, 16, v192
	v_and_b32_e32 v19, 0xffff0000, v192
	v_lshlrev_b32_e32 v14, 16, v193
	v_and_b32_e32 v15, 0xffff0000, v193
	v_lshlrev_b32_e32 v20, 16, v194
	v_and_b32_e32 v21, 0xffff0000, v194
	v_lshlrev_b32_e32 v16, 16, v195
	v_and_b32_e32 v17, 0xffff0000, v195
	v_pk_add_f32 v[10:11], v[10:11], v[14:15]
	v_pk_add_f32 v[12:13], v[12:13], v[18:19]
	v_pk_add_f32 v[6:7], v[6:7], v[16:17]
	v_pk_add_f32 v[8:9], v[8:9], v[20:21]

.LBB0_1387:
	v_or_b32_e32 v4, 16, v2
	v_ashrrev_i32_e32 v5, 31, v4
	v_lshlrev_b64 v[4:5], 11, v[4:5]
	v_lshl_add_u64 v[4:5], v[4:5], 0, s[10:11]
	v_readlane_b32 s64, v237, 61
	v_or_b32_e32 v6, v4, v170
	v_mov_b32_e32 v7, v5
	v_readlane_b32 s70, v238, 3
	v_readlane_b32 s71, v238, 4
	v_pk_mul_f32 v[10:11], v[144:145], s[22:23] op_sel_hi:[1,0]
	v_pk_mul_f32 v[14:15], v[142:143], s[22:23] op_sel_hi:[1,0]
	v_lshl_add_u64 v[8:9], s[70:71], 0, v[6:7]
	global_load_dwordx2 v[8:9], v[8:9], off
	v_lshl_add_u64 v[196:197], v[6:7], 1, s[62:63]
	global_load_dwordx4 v[192:195], v[196:197], off
	v_pk_mul_f32 v[16:17], v[140:141], s[22:23] op_sel_hi:[1,0]
	v_pk_mul_f32 v[18:19], v[138:139], s[22:23] op_sel_hi:[1,0]
	s_and_b64 vcc, exec, s[2:3]
	v_readlane_b32 s65, v237, 62
	v_readlane_b32 s66, v237, 63
	v_readlane_b32 s67, v238, 0
	v_readlane_b32 s68, v238, 1
	v_readlane_b32 s69, v238, 2
	v_readlane_b32 s72, v238, 5
	v_readlane_b32 s73, v238, 6
	v_readlane_b32 s74, v238, 7
	v_readlane_b32 s75, v238, 8
	v_readlane_b32 s76, v238, 9
	v_readlane_b32 s77, v238, 10
	v_readlane_b32 s78, v238, 11
	v_readlane_b32 s79, v238, 12
	s_waitcnt vmcnt(0)
	v_cvt_pk_f32_fp8_sdwa v[12:13], v8 src0_sel:WORD_1
	v_cvt_pk_f32_fp8_e32 v[20:21], v8
	v_cvt_pk_f32_fp8_sdwa v[22:23], v9 src0_sel:WORD_1
	v_cvt_pk_f32_fp8_e32 v[24:25], v9
	v_pk_mul_f32 v[12:13], v[10:11], v[12:13]
	v_pk_mul_f32 v[14:15], v[14:15], v[20:21]
	v_pk_mul_f32 v[8:9], v[16:17], v[22:23]
	v_pk_mul_f32 v[10:11], v[18:19], v[24:25]
	s_cbranch_vccnz .LBB0_1389
	v_lshlrev_b32_e32 v20, 16, v192
	v_and_b32_e32 v21, 0xffff0000, v192
	v_lshlrev_b32_e32 v16, 16, v193
	v_and_b32_e32 v17, 0xffff0000, v193
	v_lshlrev_b32_e32 v22, 16, v194
	v_and_b32_e32 v23, 0xffff0000, v194
	v_lshlrev_b32_e32 v18, 16, v195
	v_and_b32_e32 v19, 0xffff0000, v195
	v_pk_add_f32 v[12:13], v[12:13], v[16:17]
	v_pk_add_f32 v[14:15], v[14:15], v[20:21]
	v_pk_add_f32 v[8:9], v[8:9], v[18:19]
	v_pk_add_f32 v[10:11], v[10:11], v[22:23]

.LBB0_1392:
	v_readlane_b32 s64, v237, 61
	v_lshl_add_u64 v[4:5], v[4:5], 0, v[170:171]
	v_readlane_b32 s70, v238, 3
	v_readlane_b32 s71, v238, 4
	v_pk_mul_f32 v[8:9], v[136:137], s[22:23] op_sel_hi:[1,0]
	v_pk_mul_f32 v[12:13], v[134:135], s[22:23] op_sel_hi:[1,0]
	v_lshl_add_u64 v[6:7], s[70:71], 0, v[4:5]
	global_load_dwordx2 v[6:7], v[6:7], off offset:128
	v_lshl_add_u64 v[196:197], v[4:5], 1, s[62:63]
	global_load_dwordx4 v[192:195], v[196:197], off offset:256
	v_pk_mul_f32 v[14:15], v[132:133], s[22:23] op_sel_hi:[1,0]
	v_pk_mul_f32 v[16:17], v[130:131], s[22:23] op_sel_hi:[1,0]
	s_and_b64 vcc, exec, s[2:3]
	v_readlane_b32 s65, v237, 62
	v_readlane_b32 s66, v237, 63
	v_readlane_b32 s67, v238, 0
	v_readlane_b32 s68, v238, 1
	v_readlane_b32 s69, v238, 2
	v_readlane_b32 s72, v238, 5
	v_readlane_b32 s73, v238, 6
	v_readlane_b32 s74, v238, 7
	v_readlane_b32 s75, v238, 8
	v_readlane_b32 s76, v238, 9
	v_readlane_b32 s77, v238, 10
	v_readlane_b32 s78, v238, 11
	v_readlane_b32 s79, v238, 12
	s_waitcnt vmcnt(0)
	v_cvt_pk_f32_fp8_sdwa v[10:11], v6 src0_sel:WORD_1
	v_cvt_pk_f32_fp8_e32 v[18:19], v6
	v_cvt_pk_f32_fp8_sdwa v[20:21], v7 src0_sel:WORD_1
	v_cvt_pk_f32_fp8_e32 v[22:23], v7
	v_pk_mul_f32 v[10:11], v[8:9], v[10:11]
	v_pk_mul_f32 v[12:13], v[12:13], v[18:19]
	v_pk_mul_f32 v[6:7], v[14:15], v[20:21]
	v_pk_mul_f32 v[8:9], v[16:17], v[22:23]
	s_cbranch_vccnz .LBB0_1394
	v_lshlrev_b32_e32 v18, 16, v192
	v_and_b32_e32 v19, 0xffff0000, v192
	v_lshlrev_b32_e32 v14, 16, v193
	v_and_b32_e32 v15, 0xffff0000, v193
	v_lshlrev_b32_e32 v20, 16, v194
	v_and_b32_e32 v21, 0xffff0000, v194
	v_lshlrev_b32_e32 v16, 16, v195
	v_and_b32_e32 v17, 0xffff0000, v195
	v_pk_add_f32 v[10:11], v[10:11], v[14:15]
	v_pk_add_f32 v[12:13], v[12:13], v[18:19]
	v_pk_add_f32 v[6:7], v[6:7], v[16:17]
	v_pk_add_f32 v[8:9], v[8:9], v[20:21]

.LBB0_1397:
	v_or_b32_e32 v4, 32, v2
	v_ashrrev_i32_e32 v5, 31, v4
	v_lshlrev_b64 v[4:5], 11, v[4:5]
	v_lshl_add_u64 v[4:5], v[4:5], 0, s[10:11]
	v_readlane_b32 s64, v237, 61
	v_or_b32_e32 v6, v4, v170
	v_mov_b32_e32 v7, v5
	v_readlane_b32 s70, v238, 3
	v_readlane_b32 s71, v238, 4
	v_pk_mul_f32 v[10:11], v[128:129], s[22:23] op_sel_hi:[1,0]
	v_pk_mul_f32 v[14:15], v[126:127], s[22:23] op_sel_hi:[1,0]
	v_lshl_add_u64 v[8:9], s[70:71], 0, v[6:7]
	global_load_dwordx2 v[8:9], v[8:9], off
	v_lshl_add_u64 v[196:197], v[6:7], 1, s[62:63]
	global_load_dwordx4 v[192:195], v[196:197], off
	v_pk_mul_f32 v[16:17], v[124:125], s[22:23] op_sel_hi:[1,0]
	v_pk_mul_f32 v[18:19], v[122:123], s[22:23] op_sel_hi:[1,0]
	s_and_b64 vcc, exec, s[2:3]
	v_readlane_b32 s65, v237, 62
	v_readlane_b32 s66, v237, 63
	v_readlane_b32 s67, v238, 0
	v_readlane_b32 s68, v238, 1
	v_readlane_b32 s69, v238, 2
	v_readlane_b32 s72, v238, 5
	v_readlane_b32 s73, v238, 6
	v_readlane_b32 s74, v238, 7
	v_readlane_b32 s75, v238, 8
	v_readlane_b32 s76, v238, 9
	v_readlane_b32 s77, v238, 10
	v_readlane_b32 s78, v238, 11
	v_readlane_b32 s79, v238, 12
	s_waitcnt vmcnt(0)
	v_cvt_pk_f32_fp8_sdwa v[12:13], v8 src0_sel:WORD_1
	v_cvt_pk_f32_fp8_e32 v[20:21], v8
	v_cvt_pk_f32_fp8_sdwa v[22:23], v9 src0_sel:WORD_1
	v_cvt_pk_f32_fp8_e32 v[24:25], v9
	v_pk_mul_f32 v[12:13], v[10:11], v[12:13]
	v_pk_mul_f32 v[14:15], v[14:15], v[20:21]
	v_pk_mul_f32 v[8:9], v[16:17], v[22:23]
	v_pk_mul_f32 v[10:11], v[18:19], v[24:25]
	s_cbranch_vccnz .LBB0_1399
	v_lshlrev_b32_e32 v20, 16, v192
	v_and_b32_e32 v21, 0xffff0000, v192
	v_lshlrev_b32_e32 v16, 16, v193
	v_and_b32_e32 v17, 0xffff0000, v193
	v_lshlrev_b32_e32 v22, 16, v194
	v_and_b32_e32 v23, 0xffff0000, v194
	v_lshlrev_b32_e32 v18, 16, v195
	v_and_b32_e32 v19, 0xffff0000, v195
	v_pk_add_f32 v[12:13], v[12:13], v[16:17]
	v_pk_add_f32 v[14:15], v[14:15], v[20:21]
	v_pk_add_f32 v[8:9], v[8:9], v[18:19]
	v_pk_add_f32 v[10:11], v[10:11], v[22:23]

.LBB0_1402:
	v_readlane_b32 s64, v237, 61
	v_lshl_add_u64 v[4:5], v[4:5], 0, v[170:171]
	v_readlane_b32 s70, v238, 3
	v_readlane_b32 s71, v238, 4
	v_pk_mul_f32 v[8:9], v[120:121], s[22:23] op_sel_hi:[1,0]
	v_pk_mul_f32 v[12:13], v[118:119], s[22:23] op_sel_hi:[1,0]
	v_lshl_add_u64 v[6:7], s[70:71], 0, v[4:5]
	global_load_dwordx2 v[6:7], v[6:7], off offset:128
	v_lshl_add_u64 v[196:197], v[4:5], 1, s[62:63]
	global_load_dwordx4 v[192:195], v[196:197], off offset:256
	v_pk_mul_f32 v[14:15], v[116:117], s[22:23] op_sel_hi:[1,0]
	v_pk_mul_f32 v[16:17], v[114:115], s[22:23] op_sel_hi:[1,0]
	s_and_b64 vcc, exec, s[2:3]
	v_readlane_b32 s65, v237, 62
	v_readlane_b32 s66, v237, 63
	v_readlane_b32 s67, v238, 0
	v_readlane_b32 s68, v238, 1
	v_readlane_b32 s69, v238, 2
	v_readlane_b32 s72, v238, 5
	v_readlane_b32 s73, v238, 6
	v_readlane_b32 s74, v238, 7
	v_readlane_b32 s75, v238, 8
	v_readlane_b32 s76, v238, 9
	v_readlane_b32 s77, v238, 10
	v_readlane_b32 s78, v238, 11
	v_readlane_b32 s79, v238, 12
	s_waitcnt vmcnt(0)
	v_cvt_pk_f32_fp8_sdwa v[10:11], v6 src0_sel:WORD_1
	v_cvt_pk_f32_fp8_e32 v[18:19], v6
	v_cvt_pk_f32_fp8_sdwa v[20:21], v7 src0_sel:WORD_1
	v_cvt_pk_f32_fp8_e32 v[22:23], v7
	v_pk_mul_f32 v[10:11], v[8:9], v[10:11]
	v_pk_mul_f32 v[12:13], v[12:13], v[18:19]
	v_pk_mul_f32 v[6:7], v[14:15], v[20:21]
	v_pk_mul_f32 v[8:9], v[16:17], v[22:23]
	s_cbranch_vccnz .LBB0_1404
	v_lshlrev_b32_e32 v18, 16, v192
	v_and_b32_e32 v19, 0xffff0000, v192
	v_lshlrev_b32_e32 v14, 16, v193
	v_and_b32_e32 v15, 0xffff0000, v193
	v_lshlrev_b32_e32 v20, 16, v194
	v_and_b32_e32 v21, 0xffff0000, v194
	v_lshlrev_b32_e32 v16, 16, v195
	v_and_b32_e32 v17, 0xffff0000, v195
	v_pk_add_f32 v[10:11], v[10:11], v[14:15]
	v_pk_add_f32 v[12:13], v[12:13], v[18:19]
	v_pk_add_f32 v[6:7], v[6:7], v[16:17]
	v_pk_add_f32 v[8:9], v[8:9], v[20:21]

.LBB0_1407:
	v_or_b32_e32 v4, 48, v2
	v_ashrrev_i32_e32 v5, 31, v4
	v_lshlrev_b64 v[4:5], 11, v[4:5]
	v_lshl_add_u64 v[4:5], v[4:5], 0, s[10:11]
	v_readlane_b32 s64, v237, 61
	v_or_b32_e32 v6, v4, v170
	v_mov_b32_e32 v7, v5
	v_readlane_b32 s70, v238, 3
	v_readlane_b32 s71, v238, 4
	v_pk_mul_f32 v[10:11], v[112:113], s[22:23] op_sel_hi:[1,0]
	v_pk_mul_f32 v[14:15], v[110:111], s[22:23] op_sel_hi:[1,0]
	v_lshl_add_u64 v[8:9], s[70:71], 0, v[6:7]
	global_load_dwordx2 v[8:9], v[8:9], off
	v_lshl_add_u64 v[196:197], v[6:7], 1, s[62:63]
	global_load_dwordx4 v[192:195], v[196:197], off
	v_pk_mul_f32 v[16:17], v[108:109], s[22:23] op_sel_hi:[1,0]
	v_pk_mul_f32 v[18:19], v[106:107], s[22:23] op_sel_hi:[1,0]
	s_and_b64 vcc, exec, s[2:3]
	v_readlane_b32 s65, v237, 62
	v_readlane_b32 s66, v237, 63
	v_readlane_b32 s67, v238, 0
	v_readlane_b32 s68, v238, 1
	v_readlane_b32 s69, v238, 2
	v_readlane_b32 s72, v238, 5
	v_readlane_b32 s73, v238, 6
	v_readlane_b32 s74, v238, 7
	v_readlane_b32 s75, v238, 8
	v_readlane_b32 s76, v238, 9
	v_readlane_b32 s77, v238, 10
	v_readlane_b32 s78, v238, 11
	v_readlane_b32 s79, v238, 12
	s_waitcnt vmcnt(0)
	v_cvt_pk_f32_fp8_sdwa v[12:13], v8 src0_sel:WORD_1
	v_cvt_pk_f32_fp8_e32 v[20:21], v8
	v_cvt_pk_f32_fp8_sdwa v[22:23], v9 src0_sel:WORD_1
	v_cvt_pk_f32_fp8_e32 v[24:25], v9
	v_pk_mul_f32 v[12:13], v[10:11], v[12:13]
	v_pk_mul_f32 v[14:15], v[14:15], v[20:21]
	v_pk_mul_f32 v[8:9], v[16:17], v[22:23]
	v_pk_mul_f32 v[10:11], v[18:19], v[24:25]
	s_cbranch_vccnz .LBB0_1409
	v_lshlrev_b32_e32 v20, 16, v192
	v_and_b32_e32 v21, 0xffff0000, v192
	v_lshlrev_b32_e32 v16, 16, v193
	v_and_b32_e32 v17, 0xffff0000, v193
	v_lshlrev_b32_e32 v22, 16, v194
	v_and_b32_e32 v23, 0xffff0000, v194
	v_lshlrev_b32_e32 v18, 16, v195
	v_and_b32_e32 v19, 0xffff0000, v195
	v_pk_add_f32 v[12:13], v[12:13], v[16:17]
	v_pk_add_f32 v[14:15], v[14:15], v[20:21]
	v_pk_add_f32 v[8:9], v[8:9], v[18:19]
	v_pk_add_f32 v[10:11], v[10:11], v[22:23]

.LBB0_1412:
	v_readlane_b32 s64, v237, 61
	v_lshl_add_u64 v[4:5], v[4:5], 0, v[170:171]
	v_readlane_b32 s70, v238, 3
	v_readlane_b32 s71, v238, 4
	v_pk_mul_f32 v[8:9], v[104:105], s[22:23] op_sel_hi:[1,0]
	v_pk_mul_f32 v[12:13], v[102:103], s[22:23] op_sel_hi:[1,0]
	v_lshl_add_u64 v[6:7], s[70:71], 0, v[4:5]
	global_load_dwordx2 v[6:7], v[6:7], off offset:128
	v_lshl_add_u64 v[196:197], v[4:5], 1, s[62:63]
	global_load_dwordx4 v[192:195], v[196:197], off offset:256
	v_pk_mul_f32 v[14:15], v[100:101], s[22:23] op_sel_hi:[1,0]
	v_pk_mul_f32 v[16:17], v[98:99], s[22:23] op_sel_hi:[1,0]
	s_and_b64 vcc, exec, s[2:3]
	v_readlane_b32 s65, v237, 62
	v_readlane_b32 s66, v237, 63
	v_readlane_b32 s67, v238, 0
	v_readlane_b32 s68, v238, 1
	v_readlane_b32 s69, v238, 2
	v_readlane_b32 s72, v238, 5
	v_readlane_b32 s73, v238, 6
	v_readlane_b32 s74, v238, 7
	v_readlane_b32 s75, v238, 8
	v_readlane_b32 s76, v238, 9
	v_readlane_b32 s77, v238, 10
	v_readlane_b32 s78, v238, 11
	v_readlane_b32 s79, v238, 12
	s_waitcnt vmcnt(0)
	v_cvt_pk_f32_fp8_sdwa v[10:11], v6 src0_sel:WORD_1
	v_cvt_pk_f32_fp8_e32 v[18:19], v6
	v_cvt_pk_f32_fp8_sdwa v[20:21], v7 src0_sel:WORD_1
	v_cvt_pk_f32_fp8_e32 v[22:23], v7
	v_pk_mul_f32 v[10:11], v[8:9], v[10:11]
	v_pk_mul_f32 v[12:13], v[12:13], v[18:19]
	v_pk_mul_f32 v[6:7], v[14:15], v[20:21]
	v_pk_mul_f32 v[8:9], v[16:17], v[22:23]
	s_cbranch_vccnz .LBB0_1414
	v_lshlrev_b32_e32 v18, 16, v192
	v_and_b32_e32 v19, 0xffff0000, v192
	v_lshlrev_b32_e32 v14, 16, v193
	v_and_b32_e32 v15, 0xffff0000, v193
	v_lshlrev_b32_e32 v20, 16, v194
	v_and_b32_e32 v21, 0xffff0000, v194
	v_lshlrev_b32_e32 v16, 16, v195
	v_and_b32_e32 v17, 0xffff0000, v195
	v_pk_add_f32 v[10:11], v[10:11], v[14:15]
	v_pk_add_f32 v[12:13], v[12:13], v[18:19]
	v_pk_add_f32 v[6:7], v[6:7], v[16:17]
	v_pk_add_f32 v[8:9], v[8:9], v[20:21]

.LBB0_1417:
	v_add_u32_e32 v4, 0x80, v2
	v_ashrrev_i32_e32 v5, 31, v4
	v_lshlrev_b64 v[4:5], 11, v[4:5]
	v_lshl_add_u64 v[4:5], v[4:5], 0, s[10:11]
	v_readlane_b32 s64, v237, 61
	v_or_b32_e32 v6, v4, v170
	v_mov_b32_e32 v7, v5
	v_readlane_b32 s70, v238, 3
	v_readlane_b32 s71, v238, 4
	v_pk_mul_f32 v[10:11], v[96:97], s[22:23] op_sel_hi:[1,0]
	v_pk_mul_f32 v[14:15], v[94:95], s[22:23] op_sel_hi:[1,0]
	v_lshl_add_u64 v[8:9], s[70:71], 0, v[6:7]
	global_load_dwordx2 v[8:9], v[8:9], off
	v_lshl_add_u64 v[196:197], v[6:7], 1, s[62:63]
	global_load_dwordx4 v[192:195], v[196:197], off
	v_pk_mul_f32 v[16:17], v[92:93], s[22:23] op_sel_hi:[1,0]
	v_pk_mul_f32 v[18:19], v[90:91], s[22:23] op_sel_hi:[1,0]
	s_and_b64 vcc, exec, s[2:3]
	v_readlane_b32 s65, v237, 62
	v_readlane_b32 s66, v237, 63
	v_readlane_b32 s67, v238, 0
	v_readlane_b32 s68, v238, 1
	v_readlane_b32 s69, v238, 2
	v_readlane_b32 s72, v238, 5
	v_readlane_b32 s73, v238, 6
	v_readlane_b32 s74, v238, 7
	v_readlane_b32 s75, v238, 8
	v_readlane_b32 s76, v238, 9
	v_readlane_b32 s77, v238, 10
	v_readlane_b32 s78, v238, 11
	v_readlane_b32 s79, v238, 12
	s_waitcnt vmcnt(0)
	v_cvt_pk_f32_fp8_sdwa v[12:13], v8 src0_sel:WORD_1
	v_cvt_pk_f32_fp8_e32 v[20:21], v8
	v_cvt_pk_f32_fp8_sdwa v[22:23], v9 src0_sel:WORD_1
	v_cvt_pk_f32_fp8_e32 v[24:25], v9
	v_pk_mul_f32 v[12:13], v[10:11], v[12:13]
	v_pk_mul_f32 v[14:15], v[14:15], v[20:21]
	v_pk_mul_f32 v[8:9], v[16:17], v[22:23]
	v_pk_mul_f32 v[10:11], v[18:19], v[24:25]
	s_cbranch_vccnz .LBB0_1419
	v_lshlrev_b32_e32 v20, 16, v192
	v_and_b32_e32 v21, 0xffff0000, v192
	v_lshlrev_b32_e32 v16, 16, v193
	v_and_b32_e32 v17, 0xffff0000, v193
	v_lshlrev_b32_e32 v22, 16, v194
	v_and_b32_e32 v23, 0xffff0000, v194
	v_lshlrev_b32_e32 v18, 16, v195
	v_and_b32_e32 v19, 0xffff0000, v195
	v_pk_add_f32 v[12:13], v[12:13], v[16:17]
	v_pk_add_f32 v[14:15], v[14:15], v[20:21]
	v_pk_add_f32 v[8:9], v[8:9], v[18:19]
	v_pk_add_f32 v[10:11], v[10:11], v[22:23]

.LBB0_1422:
	v_readlane_b32 s64, v237, 61
	v_lshl_add_u64 v[4:5], v[4:5], 0, v[170:171]
	v_readlane_b32 s70, v238, 3
	v_readlane_b32 s71, v238, 4
	v_pk_mul_f32 v[8:9], v[88:89], s[22:23] op_sel_hi:[1,0]
	v_pk_mul_f32 v[12:13], v[86:87], s[22:23] op_sel_hi:[1,0]
	v_lshl_add_u64 v[6:7], s[70:71], 0, v[4:5]
	global_load_dwordx2 v[6:7], v[6:7], off offset:128
	v_lshl_add_u64 v[196:197], v[4:5], 1, s[62:63]
	global_load_dwordx4 v[192:195], v[196:197], off offset:256
	v_pk_mul_f32 v[14:15], v[84:85], s[22:23] op_sel_hi:[1,0]
	v_pk_mul_f32 v[16:17], v[82:83], s[22:23] op_sel_hi:[1,0]
	s_and_b64 vcc, exec, s[2:3]
	v_readlane_b32 s65, v237, 62
	v_readlane_b32 s66, v237, 63
	v_readlane_b32 s67, v238, 0
	v_readlane_b32 s68, v238, 1
	v_readlane_b32 s69, v238, 2
	v_readlane_b32 s72, v238, 5
	v_readlane_b32 s73, v238, 6
	v_readlane_b32 s74, v238, 7
	v_readlane_b32 s75, v238, 8
	v_readlane_b32 s76, v238, 9
	v_readlane_b32 s77, v238, 10
	v_readlane_b32 s78, v238, 11
	v_readlane_b32 s79, v238, 12
	s_waitcnt vmcnt(0)
	v_cvt_pk_f32_fp8_sdwa v[10:11], v6 src0_sel:WORD_1
	v_cvt_pk_f32_fp8_e32 v[18:19], v6
	v_cvt_pk_f32_fp8_sdwa v[20:21], v7 src0_sel:WORD_1
	v_cvt_pk_f32_fp8_e32 v[22:23], v7
	v_pk_mul_f32 v[10:11], v[8:9], v[10:11]
	v_pk_mul_f32 v[12:13], v[12:13], v[18:19]
	v_pk_mul_f32 v[6:7], v[14:15], v[20:21]
	v_pk_mul_f32 v[8:9], v[16:17], v[22:23]
	s_cbranch_vccnz .LBB0_1424
	v_lshlrev_b32_e32 v18, 16, v192
	v_and_b32_e32 v19, 0xffff0000, v192
	v_lshlrev_b32_e32 v14, 16, v193
	v_and_b32_e32 v15, 0xffff0000, v193
	v_lshlrev_b32_e32 v20, 16, v194
	v_and_b32_e32 v21, 0xffff0000, v194
	v_lshlrev_b32_e32 v16, 16, v195
	v_and_b32_e32 v17, 0xffff0000, v195
	v_pk_add_f32 v[10:11], v[10:11], v[14:15]
	v_pk_add_f32 v[12:13], v[12:13], v[18:19]
	v_pk_add_f32 v[6:7], v[6:7], v[16:17]
	v_pk_add_f32 v[8:9], v[8:9], v[20:21]

.LBB0_1427:
	v_add_u32_e32 v4, 0x90, v2
	v_ashrrev_i32_e32 v5, 31, v4
	v_lshlrev_b64 v[4:5], 11, v[4:5]
	v_lshl_add_u64 v[4:5], v[4:5], 0, s[10:11]
	v_readlane_b32 s64, v237, 61
	v_or_b32_e32 v6, v4, v170
	v_mov_b32_e32 v7, v5
	v_readlane_b32 s70, v238, 3
	v_readlane_b32 s71, v238, 4
	v_pk_mul_f32 v[10:11], v[80:81], s[22:23] op_sel_hi:[1,0]
	v_pk_mul_f32 v[14:15], v[78:79], s[22:23] op_sel_hi:[1,0]
	v_lshl_add_u64 v[8:9], s[70:71], 0, v[6:7]
	global_load_dwordx2 v[8:9], v[8:9], off
	v_lshl_add_u64 v[196:197], v[6:7], 1, s[62:63]
	global_load_dwordx4 v[192:195], v[196:197], off
	v_pk_mul_f32 v[16:17], v[76:77], s[22:23] op_sel_hi:[1,0]
	v_pk_mul_f32 v[18:19], v[74:75], s[22:23] op_sel_hi:[1,0]
	s_and_b64 vcc, exec, s[2:3]
	v_readlane_b32 s65, v237, 62
	v_readlane_b32 s66, v237, 63
	v_readlane_b32 s67, v238, 0
	v_readlane_b32 s68, v238, 1
	v_readlane_b32 s69, v238, 2
	v_readlane_b32 s72, v238, 5
	v_readlane_b32 s73, v238, 6
	v_readlane_b32 s74, v238, 7
	v_readlane_b32 s75, v238, 8
	v_readlane_b32 s76, v238, 9
	v_readlane_b32 s77, v238, 10
	v_readlane_b32 s78, v238, 11
	v_readlane_b32 s79, v238, 12
	s_waitcnt vmcnt(0)
	v_cvt_pk_f32_fp8_sdwa v[12:13], v8 src0_sel:WORD_1
	v_cvt_pk_f32_fp8_e32 v[20:21], v8
	v_cvt_pk_f32_fp8_sdwa v[22:23], v9 src0_sel:WORD_1
	v_cvt_pk_f32_fp8_e32 v[24:25], v9
	v_pk_mul_f32 v[12:13], v[10:11], v[12:13]
	v_pk_mul_f32 v[14:15], v[14:15], v[20:21]
	v_pk_mul_f32 v[8:9], v[16:17], v[22:23]
	v_pk_mul_f32 v[10:11], v[18:19], v[24:25]
	s_cbranch_vccnz .LBB0_1429
	v_lshlrev_b32_e32 v20, 16, v192
	v_and_b32_e32 v21, 0xffff0000, v192
	v_lshlrev_b32_e32 v16, 16, v193
	v_and_b32_e32 v17, 0xffff0000, v193
	v_lshlrev_b32_e32 v22, 16, v194
	v_and_b32_e32 v23, 0xffff0000, v194
	v_lshlrev_b32_e32 v18, 16, v195
	v_and_b32_e32 v19, 0xffff0000, v195
	v_pk_add_f32 v[12:13], v[12:13], v[16:17]
	v_pk_add_f32 v[14:15], v[14:15], v[20:21]
	v_pk_add_f32 v[8:9], v[8:9], v[18:19]
	v_pk_add_f32 v[10:11], v[10:11], v[22:23]

.LBB0_1432:
	v_readlane_b32 s64, v237, 61
	v_lshl_add_u64 v[4:5], v[4:5], 0, v[170:171]
	v_readlane_b32 s70, v238, 3
	v_readlane_b32 s71, v238, 4
	v_pk_mul_f32 v[8:9], v[72:73], s[22:23] op_sel_hi:[1,0]
	v_pk_mul_f32 v[12:13], v[70:71], s[22:23] op_sel_hi:[1,0]
	v_lshl_add_u64 v[6:7], s[70:71], 0, v[4:5]
	global_load_dwordx2 v[6:7], v[6:7], off offset:128
	v_lshl_add_u64 v[196:197], v[4:5], 1, s[62:63]
	global_load_dwordx4 v[192:195], v[196:197], off offset:256
	v_pk_mul_f32 v[14:15], v[68:69], s[22:23] op_sel_hi:[1,0]
	v_pk_mul_f32 v[16:17], v[66:67], s[22:23] op_sel_hi:[1,0]
	s_and_b64 vcc, exec, s[2:3]
	v_readlane_b32 s65, v237, 62
	v_readlane_b32 s66, v237, 63
	v_readlane_b32 s67, v238, 0
	v_readlane_b32 s68, v238, 1
	v_readlane_b32 s69, v238, 2
	v_readlane_b32 s72, v238, 5
	v_readlane_b32 s73, v238, 6
	v_readlane_b32 s74, v238, 7
	v_readlane_b32 s75, v238, 8
	v_readlane_b32 s76, v238, 9
	v_readlane_b32 s77, v238, 10
	v_readlane_b32 s78, v238, 11
	v_readlane_b32 s79, v238, 12
	s_waitcnt vmcnt(0)
	v_cvt_pk_f32_fp8_sdwa v[10:11], v6 src0_sel:WORD_1
	v_cvt_pk_f32_fp8_e32 v[18:19], v6
	v_cvt_pk_f32_fp8_sdwa v[20:21], v7 src0_sel:WORD_1
	v_cvt_pk_f32_fp8_e32 v[22:23], v7
	v_pk_mul_f32 v[10:11], v[8:9], v[10:11]
	v_pk_mul_f32 v[12:13], v[12:13], v[18:19]
	v_pk_mul_f32 v[6:7], v[14:15], v[20:21]
	v_pk_mul_f32 v[8:9], v[16:17], v[22:23]
	s_cbranch_vccnz .LBB0_1434
	v_lshlrev_b32_e32 v18, 16, v192
	v_and_b32_e32 v19, 0xffff0000, v192
	v_lshlrev_b32_e32 v14, 16, v193
	v_and_b32_e32 v15, 0xffff0000, v193
	v_lshlrev_b32_e32 v20, 16, v194
	v_and_b32_e32 v21, 0xffff0000, v194
	v_lshlrev_b32_e32 v16, 16, v195
	v_and_b32_e32 v17, 0xffff0000, v195
	v_pk_add_f32 v[10:11], v[10:11], v[14:15]
	v_pk_add_f32 v[12:13], v[12:13], v[18:19]
	v_pk_add_f32 v[6:7], v[6:7], v[16:17]
	v_pk_add_f32 v[8:9], v[8:9], v[20:21]

.LBB0_1437:
	v_add_u32_e32 v4, 0xa0, v2
	v_ashrrev_i32_e32 v5, 31, v4
	v_lshlrev_b64 v[4:5], 11, v[4:5]
	v_lshl_add_u64 v[4:5], v[4:5], 0, s[10:11]
	v_readlane_b32 s64, v237, 61
	v_or_b32_e32 v6, v4, v170
	v_mov_b32_e32 v7, v5
	v_readlane_b32 s70, v238, 3
	v_readlane_b32 s71, v238, 4
	v_pk_mul_f32 v[10:11], v[64:65], s[22:23] op_sel_hi:[1,0]
	v_pk_mul_f32 v[14:15], v[62:63], s[22:23] op_sel_hi:[1,0]
	v_lshl_add_u64 v[8:9], s[70:71], 0, v[6:7]
	global_load_dwordx2 v[8:9], v[8:9], off
	v_lshl_add_u64 v[196:197], v[6:7], 1, s[62:63]
	global_load_dwordx4 v[192:195], v[196:197], off
	v_pk_mul_f32 v[16:17], v[60:61], s[22:23] op_sel_hi:[1,0]
	v_pk_mul_f32 v[18:19], v[58:59], s[22:23] op_sel_hi:[1,0]
	s_and_b64 vcc, exec, s[2:3]
	v_readlane_b32 s65, v237, 62
	v_readlane_b32 s66, v237, 63
	v_readlane_b32 s67, v238, 0
	v_readlane_b32 s68, v238, 1
	v_readlane_b32 s69, v238, 2
	v_readlane_b32 s72, v238, 5
	v_readlane_b32 s73, v238, 6
	v_readlane_b32 s74, v238, 7
	v_readlane_b32 s75, v238, 8
	v_readlane_b32 s76, v238, 9
	v_readlane_b32 s77, v238, 10
	v_readlane_b32 s78, v238, 11
	v_readlane_b32 s79, v238, 12
	s_waitcnt vmcnt(0)
	v_cvt_pk_f32_fp8_sdwa v[12:13], v8 src0_sel:WORD_1
	v_cvt_pk_f32_fp8_e32 v[20:21], v8
	v_cvt_pk_f32_fp8_sdwa v[22:23], v9 src0_sel:WORD_1
	v_cvt_pk_f32_fp8_e32 v[24:25], v9
	v_pk_mul_f32 v[12:13], v[10:11], v[12:13]
	v_pk_mul_f32 v[14:15], v[14:15], v[20:21]
	v_pk_mul_f32 v[8:9], v[16:17], v[22:23]
	v_pk_mul_f32 v[10:11], v[18:19], v[24:25]
	s_cbranch_vccnz .LBB0_1439
	v_lshlrev_b32_e32 v20, 16, v192
	v_and_b32_e32 v21, 0xffff0000, v192
	v_lshlrev_b32_e32 v16, 16, v193
	v_and_b32_e32 v17, 0xffff0000, v193
	v_lshlrev_b32_e32 v22, 16, v194
	v_and_b32_e32 v23, 0xffff0000, v194
	v_lshlrev_b32_e32 v18, 16, v195
	v_and_b32_e32 v19, 0xffff0000, v195
	v_pk_add_f32 v[12:13], v[12:13], v[16:17]
	v_pk_add_f32 v[14:15], v[14:15], v[20:21]
	v_pk_add_f32 v[8:9], v[8:9], v[18:19]
	v_pk_add_f32 v[10:11], v[10:11], v[22:23]

.LBB0_1442:
	v_readlane_b32 s64, v237, 61
	v_lshl_add_u64 v[4:5], v[4:5], 0, v[170:171]
	v_readlane_b32 s70, v238, 3
	v_readlane_b32 s71, v238, 4
	v_pk_mul_f32 v[8:9], v[56:57], s[22:23] op_sel_hi:[1,0]
	v_pk_mul_f32 v[12:13], v[54:55], s[22:23] op_sel_hi:[1,0]
	v_lshl_add_u64 v[6:7], s[70:71], 0, v[4:5]
	global_load_dwordx2 v[6:7], v[6:7], off offset:128
	v_lshl_add_u64 v[196:197], v[4:5], 1, s[62:63]
	global_load_dwordx4 v[192:195], v[196:197], off offset:256
	v_pk_mul_f32 v[14:15], v[52:53], s[22:23] op_sel_hi:[1,0]
	v_pk_mul_f32 v[16:17], v[50:51], s[22:23] op_sel_hi:[1,0]
	s_and_b64 vcc, exec, s[2:3]
	v_readlane_b32 s65, v237, 62
	v_readlane_b32 s66, v237, 63
	v_readlane_b32 s67, v238, 0
	v_readlane_b32 s68, v238, 1
	v_readlane_b32 s69, v238, 2
	v_readlane_b32 s72, v238, 5
	v_readlane_b32 s73, v238, 6
	v_readlane_b32 s74, v238, 7
	v_readlane_b32 s75, v238, 8
	v_readlane_b32 s76, v238, 9
	v_readlane_b32 s77, v238, 10
	v_readlane_b32 s78, v238, 11
	v_readlane_b32 s79, v238, 12
	s_waitcnt vmcnt(0)
	v_cvt_pk_f32_fp8_sdwa v[10:11], v6 src0_sel:WORD_1
	v_cvt_pk_f32_fp8_e32 v[18:19], v6
	v_cvt_pk_f32_fp8_sdwa v[20:21], v7 src0_sel:WORD_1
	v_cvt_pk_f32_fp8_e32 v[22:23], v7
	v_pk_mul_f32 v[10:11], v[8:9], v[10:11]
	v_pk_mul_f32 v[12:13], v[12:13], v[18:19]
	v_pk_mul_f32 v[6:7], v[14:15], v[20:21]
	v_pk_mul_f32 v[8:9], v[16:17], v[22:23]
	s_cbranch_vccnz .LBB0_1444
	v_lshlrev_b32_e32 v18, 16, v192
	v_and_b32_e32 v19, 0xffff0000, v192
	v_lshlrev_b32_e32 v14, 16, v193
	v_and_b32_e32 v15, 0xffff0000, v193
	v_lshlrev_b32_e32 v20, 16, v194
	v_and_b32_e32 v21, 0xffff0000, v194
	v_lshlrev_b32_e32 v16, 16, v195
	v_and_b32_e32 v17, 0xffff0000, v195
	v_pk_add_f32 v[10:11], v[10:11], v[14:15]
	v_pk_add_f32 v[12:13], v[12:13], v[18:19]
	v_pk_add_f32 v[6:7], v[6:7], v[16:17]
	v_pk_add_f32 v[8:9], v[8:9], v[20:21]

.LBB0_1447:
	v_add_u32_e32 v2, 0xb0, v2
	v_ashrrev_i32_e32 v3, 31, v2
	v_lshlrev_b64 v[2:3], 11, v[2:3]
	v_lshl_add_u64 v[2:3], v[2:3], 0, s[10:11]
	v_readlane_b32 s64, v237, 61
	v_or_b32_e32 v4, v2, v170
	v_mov_b32_e32 v5, v3
	v_readlane_b32 s70, v238, 3
	v_readlane_b32 s71, v238, 4
	v_pk_mul_f32 v[8:9], v[48:49], s[22:23] op_sel_hi:[1,0]
	v_pk_mul_f32 v[12:13], v[46:47], s[22:23] op_sel_hi:[1,0]
	v_lshl_add_u64 v[6:7], s[70:71], 0, v[4:5]
	global_load_dwordx2 v[6:7], v[6:7], off
	v_lshl_add_u64 v[196:197], v[4:5], 1, s[62:63]
	global_load_dwordx4 v[192:195], v[196:197], off
	v_pk_mul_f32 v[14:15], v[44:45], s[22:23] op_sel_hi:[1,0]
	v_pk_mul_f32 v[16:17], v[42:43], s[22:23] op_sel_hi:[1,0]
	s_and_b64 vcc, exec, s[2:3]
	v_readlane_b32 s65, v237, 62
	v_readlane_b32 s66, v237, 63
	v_readlane_b32 s67, v238, 0
	v_readlane_b32 s68, v238, 1
	v_readlane_b32 s69, v238, 2
	v_readlane_b32 s72, v238, 5
	v_readlane_b32 s73, v238, 6
	v_readlane_b32 s74, v238, 7
	v_readlane_b32 s75, v238, 8
	v_readlane_b32 s76, v238, 9
	v_readlane_b32 s77, v238, 10
	v_readlane_b32 s78, v238, 11
	v_readlane_b32 s79, v238, 12
	s_waitcnt vmcnt(0)
	v_cvt_pk_f32_fp8_sdwa v[10:11], v6 src0_sel:WORD_1
	v_cvt_pk_f32_fp8_e32 v[18:19], v6
	v_cvt_pk_f32_fp8_sdwa v[20:21], v7 src0_sel:WORD_1
	v_cvt_pk_f32_fp8_e32 v[22:23], v7
	v_pk_mul_f32 v[10:11], v[8:9], v[10:11]
	v_pk_mul_f32 v[12:13], v[12:13], v[18:19]
	v_pk_mul_f32 v[6:7], v[14:15], v[20:21]
	v_pk_mul_f32 v[8:9], v[16:17], v[22:23]
	s_cbranch_vccnz .LBB0_1449
	v_lshlrev_b32_e32 v18, 16, v192
	v_and_b32_e32 v19, 0xffff0000, v192
	v_lshlrev_b32_e32 v14, 16, v193
	v_and_b32_e32 v15, 0xffff0000, v193
	v_lshlrev_b32_e32 v20, 16, v194
	v_and_b32_e32 v21, 0xffff0000, v194
	v_lshlrev_b32_e32 v16, 16, v195
	v_and_b32_e32 v17, 0xffff0000, v195
	v_pk_add_f32 v[10:11], v[10:11], v[14:15]
	v_pk_add_f32 v[12:13], v[12:13], v[18:19]
	v_pk_add_f32 v[6:7], v[6:7], v[16:17]
	v_pk_add_f32 v[8:9], v[8:9], v[20:21]

.LBB0_1452:
	v_readlane_b32 s64, v237, 61
	v_lshl_add_u64 v[2:3], v[2:3], 0, v[170:171]
	v_readlane_b32 s70, v238, 3
	v_readlane_b32 s71, v238, 4
	v_pk_mul_f32 v[6:7], v[40:41], s[22:23] op_sel_hi:[1,0]
	v_pk_mul_f32 v[10:11], v[38:39], s[22:23] op_sel_hi:[1,0]
	v_lshl_add_u64 v[4:5], s[70:71], 0, v[2:3]
	global_load_dwordx2 v[4:5], v[4:5], off offset:128
	v_lshl_add_u64 v[196:197], v[2:3], 1, s[62:63]
	global_load_dwordx4 v[192:195], v[196:197], off offset:256
	v_pk_mul_f32 v[12:13], v[36:37], s[22:23] op_sel_hi:[1,0]
	v_pk_mul_f32 v[14:15], v[34:35], s[22:23] op_sel_hi:[1,0]
	s_and_b64 vcc, exec, s[2:3]
	v_readlane_b32 s65, v237, 62
	v_readlane_b32 s66, v237, 63
	v_readlane_b32 s67, v238, 0
	v_readlane_b32 s68, v238, 1
	v_readlane_b32 s69, v238, 2
	v_readlane_b32 s72, v238, 5
	v_readlane_b32 s73, v238, 6
	v_readlane_b32 s74, v238, 7
	v_readlane_b32 s75, v238, 8
	v_readlane_b32 s76, v238, 9
	v_readlane_b32 s77, v238, 10
	v_readlane_b32 s78, v238, 11
	v_readlane_b32 s79, v238, 12
	s_waitcnt vmcnt(0)
	v_cvt_pk_f32_fp8_sdwa v[8:9], v4 src0_sel:WORD_1
	v_cvt_pk_f32_fp8_e32 v[16:17], v4
	v_cvt_pk_f32_fp8_sdwa v[18:19], v5 src0_sel:WORD_1
	v_cvt_pk_f32_fp8_e32 v[20:21], v5
	v_pk_mul_f32 v[8:9], v[6:7], v[8:9]
	v_pk_mul_f32 v[10:11], v[10:11], v[16:17]
	v_pk_mul_f32 v[4:5], v[12:13], v[18:19]
	v_pk_mul_f32 v[6:7], v[14:15], v[20:21]
	s_cbranch_vccnz .LBB0_1454
	v_lshlrev_b32_e32 v16, 16, v192
	v_and_b32_e32 v17, 0xffff0000, v192
	v_lshlrev_b32_e32 v12, 16, v193
	v_and_b32_e32 v13, 0xffff0000, v193
	v_lshlrev_b32_e32 v18, 16, v194
	v_and_b32_e32 v19, 0xffff0000, v194
	v_lshlrev_b32_e32 v14, 16, v195
	v_and_b32_e32 v15, 0xffff0000, v195
	v_pk_add_f32 v[8:9], v[8:9], v[12:13]
	v_pk_add_f32 v[10:11], v[10:11], v[16:17]
	v_pk_add_f32 v[4:5], v[4:5], v[14:15]
	v_pk_add_f32 v[6:7], v[6:7], v[18:19]
